# phase 9: the epilogue's row-destination lookup (sub-list position + token entry gather) is prefetched behind the prologue loads into v210/v211 and replaces the epilogue's own gather
# baseline (speedup 1.0000x reference)
.LBB0_1083:
	s_ashr_i32 s10, s46, 31
	s_lshr_b32 s10, s10, 28
	s_add_i32 s10, s46, s10
	s_ashr_i32 s10, s10, 4
	s_mov_b64 s[98:99], exec
	s_mov_b64 exec, -1
	v_and_b32_e32 v2, 63, v250
	v_lshlrev_b32_e32 v2, 2, v2
	v_add_u32_e32 v2, 0x20000, v2
	ds_read_b32 v2, v2
	s_waitcnt lgkmcnt(0)
	v_cmp_ge_i32_e64 s[100:101], s10, v2
	s_bcnt1_i32_b64 s34, s[100:101]
	s_add_i32 s34, s34, -1
	s_mov_b64 exec, s[98:99]
	s_lshl_b32 s30, s34, 2
	s_add_i32 s30, s30, 0
	s_add_i32 s30, s30, 0x20000
	v_mov_b32_e32 v4, s30
	ds_read2_b32 v[2:3], v4 offset1:80
	ds_read_b32 v4, v4 offset:640
	s_mov_b32 s35, s11
	s_waitcnt lgkmcnt(1)
	v_readfirstlane_b32 s30, v2
	s_sub_i32 s30, s10, s30
	v_readfirstlane_b32 s31, v3
	s_lshl_b32 s47, s30, 9
	s_waitcnt lgkmcnt(0)
	v_readfirstlane_b32 s49, v4
	s_sub_i32 s30, s31, s47
	s_add_i32 s49, s49, s47
	s_min_i32 s48, s30, 0x200
	s_lshl_b64 s[30:31], s[34:35], 22
	s_add_u32 s35, s6, s30
	s_addc_u32 s50, s7, s31
	s_lshl_b32 s10, s10, 11
	s_lshl_b32 s30, s46, 7
	s_sub_i32 s30, s30, s10
	s_ashr_i32 s31, s30, 31
	v_cmp_gt_i32_e32 vcc, s48, v0
	s_lshl_b64 s[36:37], s[30:31], 2
	s_add_u32 s36, s35, s36
	v_cndmask_b32_e32 v2, 0, v0, vcc
	v_add_u32_e32 v2, s49, v2
	s_addc_u32 s37, s50, s37
	v_lshl_or_b32 v146, v2, 9, v1
	v_lshl_add_u64 v[2:3], s[36:37], 0, v[152:153]
	v_lshl_add_u64 v[154:155], v[2:3], 0, v[148:149]
	s_mov_b64 s[36:37], -1
	s_cmp_ge_i32 s38, s48
	v_lshl_add_u64 v[132:133], v[154:155], 0, s[20:21]
	v_lshl_add_u64 v[130:131], v[154:155], 0, s[22:23]
	v_lshl_add_u64 v[134:135], v[154:155], 0, s[24:25]
	v_lshl_add_u64 v[138:139], v[154:155], 0, s[26:27]
	v_lshl_add_u64 v[142:143], v[154:155], 0, s[28:29]
	s_cbranch_scc0 .LBB0_1089
	global_load_dwordx4 v[2:5], v[154:155], off sc1 nt
	s_mov_b32 m0, s39
	global_load_dwordx4 v[6:9], v[132:133], off sc1 nt
	v_lshl_add_u64 v[82:83], s[12:13], 0, v[146:147]
	global_load_lds_dwordx4 v146, s[12:13]
	global_load_dwordx4 v[66:69], v[130:131], off sc1 nt
	global_load_dwordx4 v[70:73], v[134:135], off sc1 nt
	s_mov_b32 m0, s40
	s_nop 0
	global_load_lds_dwordx4 v146, s[14:15]
	s_mul_i32 s98, s34, 0x44
	s_add_i32 s98, s98, 0x20400
	s_lshl_b32 s99, s34, 13
	v_cmp_gt_i32_e32 vcc, s48, v164
	s_and_saveexec_b64 s[100:101], vcc
	s_cbranch_execz .Lp9pf_n0
	v_add_u32_e32 v204, s47, v164
	v_mov_b32_e32 v206, s98
	ds_read_b32 v206, v206 offset:32
	s_waitcnt lgkmcnt(0)
	v_cmp_gt_i32_e32 vcc, v206, v204
	s_nop 1
	v_cndmask_b32_e64 v205, 8, 0, vcc
	v_lshl_add_u32 v206, v205, 2, s98
	ds_read_b32 v206, v206 offset:16
	v_or_b32_e32 v207, 4, v205
	s_waitcnt lgkmcnt(0)
	v_cmp_gt_i32_e32 vcc, v206, v204
	s_nop 1
	v_cndmask_b32_e32 v205, v207, v205, vcc
	v_lshl_add_u32 v206, v205, 2, s98
	ds_read_b32 v206, v206 offset:8
	v_or_b32_e32 v207, 2, v205
	s_waitcnt lgkmcnt(0)
	v_cmp_gt_i32_e32 vcc, v206, v204
	s_nop 1
	v_cndmask_b32_e32 v205, v207, v205, vcc
	v_lshl_add_u32 v206, v205, 2, s98
	ds_read_b32 v206, v206 offset:4
	v_or_b32_e32 v207, 1, v205
	s_waitcnt lgkmcnt(0)
	v_cmp_gt_i32_e32 vcc, v206, v204
	s_nop 1
	v_cndmask_b32_e32 v205, v207, v205, vcc
	v_lshl_add_u32 v206, v205, 2, s98
	ds_read_b32 v206, v206
	v_add_u32_e32 v207, s99, v204
	s_waitcnt lgkmcnt(0)
	v_sub_u32_e32 v207, v207, v206
	v_lshl_add_u32 v208, v205, 9, v207
	v_ashrrev_i32_e32 v209, 31, v208
	v_lshl_add_u64 v[208:209], v[208:209], 2, s[8:9]
	global_load_dword v210, v[208:209], off
.Lp9pf_n0:
	s_or_b64 exec, exec, s[100:101]
	v_cmp_gt_i32_e32 vcc, s48, v166
	s_and_saveexec_b64 s[100:101], vcc
	s_cbranch_execz .Lp9pf_n1
	v_add_u32_e32 v204, s47, v166
	v_mov_b32_e32 v206, s98
	ds_read_b32 v206, v206 offset:32
	s_waitcnt lgkmcnt(0)
	v_cmp_gt_i32_e32 vcc, v206, v204
	s_nop 1
	v_cndmask_b32_e64 v205, 8, 0, vcc
	v_lshl_add_u32 v206, v205, 2, s98
	ds_read_b32 v206, v206 offset:16
	v_or_b32_e32 v207, 4, v205
	s_waitcnt lgkmcnt(0)
	v_cmp_gt_i32_e32 vcc, v206, v204
	s_nop 1
	v_cndmask_b32_e32 v205, v207, v205, vcc
	v_lshl_add_u32 v206, v205, 2, s98
	ds_read_b32 v206, v206 offset:8
	v_or_b32_e32 v207, 2, v205
	s_waitcnt lgkmcnt(0)
	v_cmp_gt_i32_e32 vcc, v206, v204
	s_nop 1
	v_cndmask_b32_e32 v205, v207, v205, vcc
	v_lshl_add_u32 v206, v205, 2, s98
	ds_read_b32 v206, v206 offset:4
	v_or_b32_e32 v207, 1, v205
	s_waitcnt lgkmcnt(0)
	v_cmp_gt_i32_e32 vcc, v206, v204
	s_nop 1
	v_cndmask_b32_e32 v205, v207, v205, vcc
	v_lshl_add_u32 v206, v205, 2, s98
	ds_read_b32 v206, v206
	v_add_u32_e32 v207, s99, v204
	s_waitcnt lgkmcnt(0)
	v_sub_u32_e32 v207, v207, v206
	v_lshl_add_u32 v208, v205, 9, v207
	v_ashrrev_i32_e32 v209, 31, v208
	v_lshl_add_u64 v[208:209], v[208:209], 2, s[8:9]
	global_load_dword v211, v[208:209], off
.Lp9pf_n1:
	s_or_b64 exec, exec, s[100:101]
	s_waitcnt vmcnt(4)
	s_nop 0
	v_cvt_pk_bf16_f32 v2, v2, v6
	ds_write_b32 v167, v2 offset:49152
	v_cvt_pk_bf16_f32 v2, v3, v7
	ds_write_b32 v167, v2 offset:49216
	v_cvt_pk_bf16_f32 v2, v4, v8
	ds_write_b32 v167, v2 offset:49280
	v_cvt_pk_bf16_f32 v2, v5, v9
	ds_write_b32 v167, v2 offset:49344
	global_load_dwordx4 v[74:77], v[138:139], off sc1 nt
	global_load_dwordx4 v[78:81], v[142:143], off sc1 nt
	s_waitcnt vmcnt(5)
	s_mov_b32 m0, s41
	s_waitcnt lgkmcnt(0)
	s_barrier
	global_load_lds_dwordx4 v146, s[16:17]
	v_mov_b32_e32 v2, 0
	s_mov_b32 s36, -2
	s_movk_i32 s35, 0x80
	v_mov_b32_e32 v3, v2
	v_mov_b32_e32 v4, v2
	v_mov_b32_e32 v5, v2
	v_mov_b32_e32 v6, v2
	v_mov_b32_e32 v7, v2
	v_mov_b32_e32 v8, v2
	v_mov_b32_e32 v9, v2
	v_mov_b32_e32 v10, v2
	v_mov_b32_e32 v11, v2
	v_mov_b32_e32 v12, v2
	v_mov_b32_e32 v13, v2
	v_mov_b32_e32 v14, v2
	v_mov_b32_e32 v15, v2
	v_mov_b32_e32 v16, v2
	v_mov_b32_e32 v17, v2
	v_mov_b32_e32 v18, v2
	v_mov_b32_e32 v19, v2
	v_mov_b32_e32 v20, v2
	v_mov_b32_e32 v21, v2
	v_mov_b32_e32 v22, v2
	v_mov_b32_e32 v23, v2
	v_mov_b32_e32 v24, v2
	v_mov_b32_e32 v25, v2
	v_mov_b32_e32 v26, v2
	v_mov_b32_e32 v27, v2
	v_mov_b32_e32 v28, v2
	v_mov_b32_e32 v29, v2
	v_mov_b32_e32 v30, v2
	v_mov_b32_e32 v31, v2
	v_mov_b32_e32 v32, v2
	v_mov_b32_e32 v33, v2
	v_mov_b32_e32 v34, v2
	v_mov_b32_e32 v35, v2
	v_mov_b32_e32 v36, v2
	v_mov_b32_e32 v37, v2
	v_mov_b32_e32 v38, v2
	v_mov_b32_e32 v39, v2
	v_mov_b32_e32 v40, v2
	v_mov_b32_e32 v41, v2
	v_mov_b32_e32 v42, v2
	v_mov_b32_e32 v43, v2
	v_mov_b32_e32 v44, v2
	v_mov_b32_e32 v45, v2
	v_mov_b32_e32 v46, v2
	v_mov_b32_e32 v47, v2
	v_mov_b32_e32 v48, v2
	v_mov_b32_e32 v49, v2
	v_mov_b32_e32 v50, v2
	v_mov_b32_e32 v51, v2
	v_mov_b32_e32 v52, v2
	v_mov_b32_e32 v53, v2
	v_mov_b32_e32 v54, v2
	v_mov_b32_e32 v55, v2
	v_mov_b32_e32 v56, v2
	v_mov_b32_e32 v57, v2
	v_mov_b32_e32 v58, v2
	v_mov_b32_e32 v59, v2
	v_mov_b32_e32 v60, v2
	v_mov_b32_e32 v61, v2
	v_mov_b32_e32 v62, v2
	v_mov_b32_e32 v63, v2
	v_mov_b32_e32 v64, v2
	v_mov_b32_e32 v65, v2
	v_readfirstlane_b32 s98, v250
	s_bitcmp1_b32 s98, 6
	s_cbranch_scc1 .Lmoe_B_1087

.LBB0_1089:
	v_mov_b32_e32 v129, 0
	s_and_b64 vcc, exec, s[36:37]
	v_mov_b32_e32 v128, v129
	v_mov_b32_e32 v127, v129
	v_mov_b32_e32 v126, v129
	v_mov_b32_e32 v125, v129
	v_mov_b32_e32 v124, v129
	v_mov_b32_e32 v123, v129
	v_mov_b32_e32 v122, v129
	v_mov_b32_e32 v121, v129
	v_mov_b32_e32 v120, v129
	v_mov_b32_e32 v119, v129
	v_mov_b32_e32 v118, v129
	v_mov_b32_e32 v117, v129
	v_mov_b32_e32 v116, v129
	v_mov_b32_e32 v115, v129
	v_mov_b32_e32 v114, v129
	v_mov_b32_e32 v113, v129
	v_mov_b32_e32 v112, v129
	v_mov_b32_e32 v111, v129
	v_mov_b32_e32 v110, v129
	v_mov_b32_e32 v109, v129
	v_mov_b32_e32 v108, v129
	v_mov_b32_e32 v107, v129
	v_mov_b32_e32 v106, v129
	v_mov_b32_e32 v105, v129
	v_mov_b32_e32 v104, v129
	v_mov_b32_e32 v103, v129
	v_mov_b32_e32 v102, v129
	v_mov_b32_e32 v101, v129
	v_mov_b32_e32 v100, v129
	v_mov_b32_e32 v99, v129
	v_mov_b32_e32 v98, v129
	v_mov_b32_e32 v97, v129
	v_mov_b32_e32 v96, v129
	v_mov_b32_e32 v95, v129
	v_mov_b32_e32 v94, v129
	v_mov_b32_e32 v93, v129
	v_mov_b32_e32 v92, v129
	v_mov_b32_e32 v91, v129
	v_mov_b32_e32 v90, v129
	v_mov_b32_e32 v89, v129
	v_mov_b32_e32 v88, v129
	v_mov_b32_e32 v87, v129
	v_mov_b32_e32 v86, v129
	v_mov_b32_e32 v85, v129
	v_mov_b32_e32 v84, v129
	v_mov_b32_e32 v83, v129
	v_mov_b32_e32 v82, v129
	v_mov_b32_e32 v81, v129
	v_mov_b32_e32 v80, v129
	v_mov_b32_e32 v79, v129
	v_mov_b32_e32 v78, v129
	v_mov_b32_e32 v77, v129
	v_mov_b32_e32 v76, v129
	v_mov_b32_e32 v75, v129
	v_mov_b32_e32 v74, v129
	v_mov_b32_e32 v73, v129
	v_mov_b32_e32 v72, v129
	v_mov_b32_e32 v71, v129
	v_mov_b32_e32 v70, v129
	v_mov_b32_e32 v69, v129
	v_mov_b32_e32 v68, v129
	v_mov_b32_e32 v67, v129
	v_mov_b32_e32 v66, v129
	s_cbranch_vccz .LBB0_1093
	v_cmp_gt_i32_e32 vcc, s48, v165
	s_mov_b32 m0, s39
	v_mov_b32_e32 v157, v147
	v_cndmask_b32_e32 v2, 0, v165, vcc
	v_add_u32_e32 v2, s49, v2
	v_lshl_or_b32 v156, v2, 9, v1
	global_load_dwordx4 v[2:5], v[154:155], off sc1 nt
	global_load_dwordx4 v[6:9], v[132:133], off sc1 nt
	global_load_lds_dwordx4 v146, s[12:13]
	s_mov_b32 m0, s42
	s_nop 0
	global_load_lds_dwordx4 v156, s[12:13]
	global_load_dwordx4 v[130:133], v[130:131], off sc1 nt
	global_load_dwordx4 v[134:137], v[134:135], off sc1 nt
	s_mov_b32 m0, s40
	s_nop 0
	global_load_lds_dwordx4 v146, s[14:15]
	s_mov_b32 m0, s43
	s_nop 0
	global_load_lds_dwordx4 v156, s[14:15]
	s_mul_i32 s98, s34, 0x44
	s_add_i32 s98, s98, 0x20400
	s_lshl_b32 s99, s34, 13
	v_cmp_gt_i32_e32 vcc, s48, v164
	s_and_saveexec_b64 s[100:101], vcc
	s_cbranch_execz .Lp9pf_t0
	v_add_u32_e32 v204, s47, v164
	v_mov_b32_e32 v206, s98
	ds_read_b32 v206, v206 offset:32
	s_waitcnt lgkmcnt(0)
	v_cmp_gt_i32_e32 vcc, v206, v204
	s_nop 1
	v_cndmask_b32_e64 v205, 8, 0, vcc
	v_lshl_add_u32 v206, v205, 2, s98
	ds_read_b32 v206, v206 offset:16
	v_or_b32_e32 v207, 4, v205
	s_waitcnt lgkmcnt(0)
	v_cmp_gt_i32_e32 vcc, v206, v204
	s_nop 1
	v_cndmask_b32_e32 v205, v207, v205, vcc
	v_lshl_add_u32 v206, v205, 2, s98
	ds_read_b32 v206, v206 offset:8
	v_or_b32_e32 v207, 2, v205
	s_waitcnt lgkmcnt(0)
	v_cmp_gt_i32_e32 vcc, v206, v204
	s_nop 1
	v_cndmask_b32_e32 v205, v207, v205, vcc
	v_lshl_add_u32 v206, v205, 2, s98
	ds_read_b32 v206, v206 offset:4
	v_or_b32_e32 v207, 1, v205
	s_waitcnt lgkmcnt(0)
	v_cmp_gt_i32_e32 vcc, v206, v204
	s_nop 1
	v_cndmask_b32_e32 v205, v207, v205, vcc
	v_lshl_add_u32 v206, v205, 2, s98
	ds_read_b32 v206, v206
	v_add_u32_e32 v207, s99, v204
	s_waitcnt lgkmcnt(0)
	v_sub_u32_e32 v207, v207, v206
	v_lshl_add_u32 v208, v205, 9, v207
	v_ashrrev_i32_e32 v209, 31, v208
	v_lshl_add_u64 v[208:209], v[208:209], 2, s[8:9]
	global_load_dword v210, v[208:209], off

.Lp9pf_t1:
	s_or_b64 exec, exec, s[100:101]
	s_waitcnt vmcnt(6)
	s_nop 0
	v_cvt_pk_bf16_f32 v2, v2, v6
	ds_write_b32 v167, v2 offset:49152
	v_cvt_pk_bf16_f32 v2, v3, v7
	ds_write_b32 v167, v2 offset:49216
	v_cvt_pk_bf16_f32 v2, v4, v8
	ds_write_b32 v167, v2 offset:49280
	v_cvt_pk_bf16_f32 v2, v5, v9
	ds_write_b32 v167, v2 offset:49344
	global_load_dwordx4 v[138:141], v[138:139], off sc1 nt
	global_load_dwordx4 v[142:145], v[142:143], off sc1 nt
	s_waitcnt vmcnt(6)
	s_mov_b32 m0, s41
	s_waitcnt lgkmcnt(0)
	s_barrier
	global_load_lds_dwordx4 v146, s[16:17]
	s_mov_b32 m0, s44
	v_mov_b32_e32 v66, 0
	global_load_lds_dwordx4 v156, s[16:17]
	s_mov_b32 s36, -2
	s_movk_i32 s35, 0x80
	v_mov_b32_e32 v67, v66
	v_mov_b32_e32 v68, v66
	v_mov_b32_e32 v69, v66
	v_mov_b32_e32 v70, v66
	v_mov_b32_e32 v71, v66
	v_mov_b32_e32 v72, v66
	v_mov_b32_e32 v73, v66
	v_mov_b32_e32 v74, v66
	v_mov_b32_e32 v75, v66
	v_mov_b32_e32 v76, v66
	v_mov_b32_e32 v77, v66
	v_mov_b32_e32 v78, v66
	v_mov_b32_e32 v79, v66
	v_mov_b32_e32 v80, v66
	v_mov_b32_e32 v81, v66
	v_mov_b32_e32 v82, v66
	v_mov_b32_e32 v83, v66
	v_mov_b32_e32 v84, v66
	v_mov_b32_e32 v85, v66
	v_mov_b32_e32 v86, v66
	v_mov_b32_e32 v87, v66
	v_mov_b32_e32 v88, v66
	v_mov_b32_e32 v89, v66
	v_mov_b32_e32 v90, v66
	v_mov_b32_e32 v91, v66
	v_mov_b32_e32 v92, v66
	v_mov_b32_e32 v93, v66
	v_mov_b32_e32 v94, v66
	v_mov_b32_e32 v95, v66
	v_mov_b32_e32 v96, v66
	v_mov_b32_e32 v97, v66
	v_mov_b32_e32 v98, v66
	v_mov_b32_e32 v99, v66
	v_mov_b32_e32 v100, v66
	v_mov_b32_e32 v101, v66
	v_mov_b32_e32 v102, v66
	v_mov_b32_e32 v103, v66
	v_mov_b32_e32 v104, v66
	v_mov_b32_e32 v105, v66
	v_mov_b32_e32 v106, v66
	v_mov_b32_e32 v107, v66
	v_mov_b32_e32 v108, v66
	v_mov_b32_e32 v109, v66
	v_mov_b32_e32 v110, v66
	v_mov_b32_e32 v111, v66
	v_mov_b32_e32 v112, v66
	v_mov_b32_e32 v113, v66
	v_mov_b32_e32 v114, v66
	v_mov_b32_e32 v115, v66
	v_mov_b32_e32 v116, v66
	v_mov_b32_e32 v117, v66
	v_mov_b32_e32 v118, v66
	v_mov_b32_e32 v119, v66
	v_mov_b32_e32 v120, v66
	v_mov_b32_e32 v121, v66
	v_mov_b32_e32 v122, v66
	v_mov_b32_e32 v123, v66
	v_mov_b32_e32 v124, v66
	v_mov_b32_e32 v125, v66
	v_mov_b32_e32 v126, v66
	v_mov_b32_e32 v127, v66
	v_mov_b32_e32 v128, v66
	v_mov_b32_e32 v129, v66
	v_mov_b32_e32 v2, v66
	v_mov_b32_e32 v3, v66
	v_mov_b32_e32 v4, v66
	v_mov_b32_e32 v5, v66
	v_mov_b32_e32 v6, v66
	v_mov_b32_e32 v7, v66
	v_mov_b32_e32 v8, v66
	v_mov_b32_e32 v9, v66
	v_mov_b32_e32 v10, v66
	v_mov_b32_e32 v11, v66
	v_mov_b32_e32 v12, v66
	v_mov_b32_e32 v13, v66
	v_mov_b32_e32 v14, v66
	v_mov_b32_e32 v15, v66
	v_mov_b32_e32 v16, v66
	v_mov_b32_e32 v17, v66
	v_mov_b32_e32 v18, v66
	v_mov_b32_e32 v19, v66
	v_mov_b32_e32 v20, v66
	v_mov_b32_e32 v21, v66
	v_mov_b32_e32 v22, v66
	v_mov_b32_e32 v23, v66
	v_mov_b32_e32 v24, v66
	v_mov_b32_e32 v25, v66
	v_mov_b32_e32 v26, v66
	v_mov_b32_e32 v27, v66
	v_mov_b32_e32 v28, v66
	v_mov_b32_e32 v29, v66
	v_mov_b32_e32 v30, v66
	v_mov_b32_e32 v31, v66
	v_mov_b32_e32 v32, v66
	v_mov_b32_e32 v33, v66
	v_mov_b32_e32 v34, v66
	v_mov_b32_e32 v35, v66
	v_mov_b32_e32 v36, v66
	v_mov_b32_e32 v37, v66
	v_mov_b32_e32 v38, v66
	v_mov_b32_e32 v39, v66
	v_mov_b32_e32 v40, v66
	v_mov_b32_e32 v41, v66
	v_mov_b32_e32 v42, v66
	v_mov_b32_e32 v43, v66
	v_mov_b32_e32 v44, v66
	v_mov_b32_e32 v45, v66
	v_mov_b32_e32 v46, v66
	v_mov_b32_e32 v47, v66
	v_mov_b32_e32 v48, v66
	v_mov_b32_e32 v49, v66
	v_mov_b32_e32 v50, v66
	v_mov_b32_e32 v51, v66
	v_mov_b32_e32 v52, v66
	v_mov_b32_e32 v53, v66
	v_mov_b32_e32 v54, v66
	v_mov_b32_e32 v55, v66
	v_mov_b32_e32 v56, v66
	v_mov_b32_e32 v57, v66
	v_mov_b32_e32 v58, v66
	v_mov_b32_e32 v59, v66
	v_mov_b32_e32 v60, v66
	v_mov_b32_e32 v61, v66
	v_mov_b32_e32 v62, v66
	v_mov_b32_e32 v63, v66
	v_mov_b32_e32 v64, v66
	v_mov_b32_e32 v65, v66
	v_readfirstlane_b32 s98, v250
	s_bitcmp1_b32 s98, 6
	s_cbranch_scc1 .Lmoe_B_1091

.LBB0_1093:
	s_waitcnt vmcnt(0)
	s_lshl_b32 s10, s34, 13
	s_mulk_i32 s34, 0x44
	s_add_i32 s36, s34, 0
	s_add_i32 s36, s36, 0x20400
	v_cmp_gt_i32_e32 vcc, s48, v164
	s_and_saveexec_b64 s[34:35], vcc
	s_cbranch_execz .LBB0_1095
	v_mov_b32_e32 v130, s36
	ds_read_b32 v130, v130 offset:32
	v_add_u32_e32 v131, s47, v164
	v_med3_f32 v134, v51, s45, v168
	v_med3_f32 v135, v53, s45, v168
	v_add_u32_e32 v53, s10, v131
	s_waitcnt lgkmcnt(0)
	v_cmp_gt_i32_e32 vcc, v130, v131
	v_med3_f32 v139, v18, s45, v168
	v_med3_f32 v140, v19, s45, v168
	v_cndmask_b32_e64 v130, 8, 0, vcc
	v_lshl_add_u32 v132, v130, 2, s36
	ds_read_b32 v132, v132 offset:16
	v_or_b32_e32 v133, 4, v130
	v_mov_b32_e32 v18, v147
	v_cvt_pk_fp8_f32 v18, v139, v140
	v_med3_f32 v20, v20, s45, v168
	s_waitcnt lgkmcnt(0)
	v_cmp_gt_i32_e32 vcc, v132, v131
	v_med3_f32 v21, v21, s45, v168
	v_cvt_pk_fp8_f32 v18, v20, v21 op_sel:[0,0,1]
	v_cndmask_b32_e32 v130, v133, v130, vcc
	v_lshl_add_u32 v132, v130, 2, s36
	ds_read_b32 v132, v132 offset:8
	v_med3_f32 v133, v50, s45, v168
	v_or_b32_e32 v50, 2, v130
	v_med3_f32 v22, v22, s45, v168
	v_med3_f32 v23, v23, s45, v168
	s_waitcnt lgkmcnt(0)
	v_cmp_gt_i32_e32 vcc, v132, v131
	v_med3_f32 v132, v52, s45, v168
	v_mov_b32_e32 v19, v147
	v_cndmask_b32_e32 v51, v50, v130, vcc
	v_lshl_add_u32 v50, v51, 2, s36
	ds_read_b32 v130, v50 offset:4
	v_or_b32_e32 v52, 1, v51
	v_cvt_pk_fp8_f32 v19, v22, v23
	v_med3_f32 v26, v26, s45, v168
	v_mov_b32_e32 v50, v147
	s_waitcnt lgkmcnt(0)
	v_cmp_gt_i32_e32 vcc, v130, v131
	v_med3_f32 v54, v54, s45, v168
	v_med3_f32 v55, v55, s45, v168
	v_cndmask_b32_e32 v51, v52, v51, vcc
	v_lshl_add_u32 v52, v51, 2, s36
	ds_read_b32 v52, v52
	v_med3_f32 v58, v58, s45, v168
	v_med3_f32 v59, v59, s45, v168
	v_med3_f32 v62, v62, s45, v168
	v_med3_f32 v63, v63, s45, v168
	s_waitcnt lgkmcnt(0)
	v_sub_u32_e32 v52, v53, v52
	v_lshl_add_u32 v52, v51, 9, v52
	v_ashrrev_i32_e32 v53, 31, v52
	v_lshl_add_u64 v[52:53], v[52:53], 2, s[8:9]
	v_mov_b32_e32 v130, v210
	v_mov_b32_e32 v51, v147
	v_mov_b32_e32 v52, v147
	v_mov_b32_e32 v53, v147
	v_med3_f32 v131, v34, s45, v168
	v_med3_f32 v136, v35, s45, v168
	v_med3_f32 v137, v36, s45, v168
	v_med3_f32 v138, v37, s45, v168
	v_mov_b32_e32 v34, v147
	v_med3_f32 v38, v38, s45, v168
	v_med3_f32 v39, v39, s45, v168
	v_mov_b32_e32 v35, v147
	v_med3_f32 v42, v42, s45, v168
	v_med3_f32 v43, v43, s45, v168
	v_mov_b32_e32 v36, v147
	v_med3_f32 v46, v46, s45, v168
	v_med3_f32 v47, v47, s45, v168
	v_mov_b32_e32 v37, v147
	v_cvt_pk_fp8_f32 v50, v133, v134
	v_cvt_pk_fp8_f32 v51, v54, v55
	v_cvt_pk_fp8_f32 v52, v58, v59
	v_cvt_pk_fp8_f32 v53, v62, v63
	v_med3_f32 v24, v24, s45, v168
	v_med3_f32 v25, v25, s45, v168
	v_cvt_pk_fp8_f32 v34, v131, v136
	v_cvt_pk_fp8_f32 v35, v38, v39
	v_cvt_pk_fp8_f32 v36, v42, v43
	v_cvt_pk_fp8_f32 v37, v46, v47
	v_cvt_pk_fp8_f32 v19, v24, v25 op_sel:[0,0,1]
	v_med3_f32 v24, v28, s45, v168
	v_med3_f32 v25, v29, s45, v168
	v_med3_f32 v56, v56, s45, v168
	v_med3_f32 v57, v57, s45, v168
	v_med3_f32 v60, v60, s45, v168
	v_med3_f32 v61, v61, s45, v168
	v_med3_f32 v64, v64, s45, v168
	v_med3_f32 v65, v65, s45, v168
	v_med3_f32 v40, v40, s45, v168
	v_med3_f32 v41, v41, s45, v168
	v_med3_f32 v44, v44, s45, v168
	v_med3_f32 v45, v45, s45, v168
	v_med3_f32 v48, v48, s45, v168
	v_med3_f32 v49, v49, s45, v168
	v_cvt_pk_fp8_f32 v50, v132, v135 op_sel:[0,0,1]
	v_cvt_pk_fp8_f32 v51, v56, v57 op_sel:[0,0,1]
	v_cvt_pk_fp8_f32 v52, v60, v61 op_sel:[0,0,1]
	v_cvt_pk_fp8_f32 v53, v64, v65 op_sel:[0,0,1]
	v_cvt_pk_fp8_f32 v34, v137, v138 op_sel:[0,0,1]
	v_cvt_pk_fp8_f32 v35, v40, v41 op_sel:[0,0,1]
	v_cvt_pk_fp8_f32 v36, v44, v45 op_sel:[0,0,1]
	v_cvt_pk_fp8_f32 v37, v48, v49 op_sel:[0,0,1]
	v_permlane32_swap_b32_e32 v50, v51
	v_permlane32_swap_b32_e32 v52, v53
	v_permlane32_swap_b32_e32 v18, v19
	v_permlane32_swap_b32_e32 v34, v35
	v_permlane32_swap_b32_e32 v36, v37
	v_permlane32_swap_b32_e32 v50, v52
	v_permlane32_swap_b32_e32 v51, v53
	v_permlane32_swap_b32_e32 v34, v36
	v_permlane32_swap_b32_e32 v35, v37
	v_med3_f32 v3, v3, s45, v168
	v_med3_f32 v6, v6, s45, v168
	v_med3_f32 v7, v7, s45, v168
	v_med3_f32 v4, v4, s45, v168
	v_med3_f32 v5, v5, s45, v168
	s_waitcnt vmcnt(0)
	v_ashrrev_i32_e32 v20, 16, v130
	v_ashrrev_i32_e32 v21, 31, v20
	v_lshlrev_b32_e32 v22, 11, v130
	v_lshlrev_b64 v[20:21], 24, v[20:21]
	v_and_b32_e32 v146, 0x7fff800, v22
	v_lshl_add_u64 v[20:21], s[18:19], 0, v[20:21]
	v_lshl_add_u64 v[20:21], v[20:21], 0, v[146:147]
	v_lshl_add_u64 v[20:21], v[20:21], 0, s[30:31]
	v_lshl_add_u64 v[22:23], v[20:21], 0, v[150:151]
	v_med3_f32 v21, v27, s45, v168
	v_mov_b32_e32 v20, v147
	v_cvt_pk_fp8_f32 v20, v26, v21
	v_med3_f32 v26, v30, s45, v168
	v_med3_f32 v27, v31, s45, v168
	v_mov_b32_e32 v21, v147
	v_cvt_pk_fp8_f32 v21, v26, v27
	v_cvt_pk_fp8_f32 v20, v24, v25 op_sel:[0,0,1]
	v_med3_f32 v24, v32, s45, v168
	v_med3_f32 v25, v33, s45, v168
	v_cvt_pk_fp8_f32 v21, v24, v25 op_sel:[0,0,1]
	global_store_dwordx4 v[22:23], v[50:53], off
	global_store_dwordx4 v[22:23], v[34:37], off offset:32
	v_permlane32_swap_b32_e32 v20, v21
	s_nop 1
	v_permlane32_swap_b32_e32 v18, v20
	v_permlane32_swap_b32_e32 v19, v21
	global_store_dwordx4 v[22:23], v[18:21], off offset:64
	s_nop 1
	v_med3_f32 v18, v2, s45, v168
	v_mov_b32_e32 v2, v147
	v_cvt_pk_fp8_f32 v2, v18, v3
	v_mov_b32_e32 v3, v147
	v_cvt_pk_fp8_f32 v3, v6, v7
	v_med3_f32 v6, v11, s45, v168
	v_cvt_pk_fp8_f32 v2, v4, v5 op_sel:[0,0,1]
	v_med3_f32 v4, v8, s45, v168
	v_med3_f32 v5, v9, s45, v168
	v_cvt_pk_fp8_f32 v3, v4, v5 op_sel:[0,0,1]
	v_med3_f32 v5, v10, s45, v168
	v_mov_b32_e32 v4, v147
	v_cvt_pk_fp8_f32 v4, v5, v6
	v_med3_f32 v6, v14, s45, v168
	v_med3_f32 v9, v15, s45, v168
	v_mov_b32_e32 v5, v147
	v_cvt_pk_fp8_f32 v5, v6, v9
	v_med3_f32 v7, v12, s45, v168
	v_med3_f32 v8, v13, s45, v168
	v_cvt_pk_fp8_f32 v4, v7, v8 op_sel:[0,0,1]
	v_med3_f32 v6, v16, s45, v168
	v_med3_f32 v7, v17, s45, v168
	v_cvt_pk_fp8_f32 v5, v6, v7 op_sel:[0,0,1]
	v_permlane32_swap_b32_e32 v2, v3
	s_nop 0
	v_permlane32_swap_b32_e32 v4, v5
	s_nop 1
	v_permlane32_swap_b32_e32 v2, v4
	v_permlane32_swap_b32_e32 v3, v5
	global_store_dwordx4 v[22:23], v[2:5], off offset:96
.LBB0_1095:
	s_or_b64 exec, exec, s[34:35]
	v_cmp_gt_i32_e32 vcc, s48, v166
	s_and_saveexec_b64 s[34:35], vcc
	s_cbranch_execz .LBB0_1082
	v_mov_b32_e32 v2, s36
	ds_read_b32 v2, v2 offset:32
	v_add_u32_e32 v3, s47, v166
	v_med3_f32 v12, v114, s45, v168
	v_med3_f32 v13, v115, s45, v168
	v_med3_f32 v16, v118, s45, v168
	s_waitcnt lgkmcnt(0)
	v_cmp_gt_i32_e32 vcc, v2, v3
	v_med3_f32 v17, v119, s45, v168
	v_med3_f32 v21, v122, s45, v168
	v_cndmask_b32_e64 v2, 8, 0, vcc
	v_lshl_add_u32 v4, v2, 2, s36
	ds_read_b32 v4, v4 offset:16
	v_or_b32_e32 v5, 4, v2
	v_med3_f32 v22, v123, s45, v168
	v_med3_f32 v25, v126, s45, v168
	v_med3_f32 v26, v127, s45, v168
	s_waitcnt lgkmcnt(0)
	v_cmp_gt_i32_e32 vcc, v4, v3
	v_med3_f32 v29, v98, s45, v168
	v_med3_f32 v30, v99, s45, v168
	v_cndmask_b32_e32 v2, v5, v2, vcc
	v_lshl_add_u32 v4, v2, 2, s36
	ds_read_b32 v4, v4 offset:8
	v_or_b32_e32 v5, 2, v2
	v_med3_f32 v33, v102, s45, v168
	v_med3_f32 v34, v103, s45, v168
	v_mov_b32_e32 v7, v147
	s_waitcnt lgkmcnt(0)
	v_cmp_gt_i32_e32 vcc, v4, v3
	v_med3_f32 v37, v106, s45, v168
	v_med3_f32 v38, v107, s45, v168
	v_cndmask_b32_e32 v4, v5, v2, vcc
	v_lshl_add_u32 v2, v4, 2, s36
	ds_read_b32 v5, v2 offset:4
	v_or_b32_e32 v6, 1, v4
	v_mov_b32_e32 v2, v147
	v_mov_b32_e32 v8, v147
	v_med3_f32 v41, v110, s45, v168
	s_waitcnt lgkmcnt(0)
	v_cmp_gt_i32_e32 vcc, v5, v3
	v_add_u32_e32 v3, s10, v3
	v_med3_f32 v42, v111, s45, v168
	v_cndmask_b32_e32 v4, v6, v4, vcc
	v_lshl_add_u32 v5, v4, 2, s36
	ds_read_b32 v5, v5
	v_mov_b32_e32 v6, v147
	v_mov_b32_e32 v9, v147
	v_cvt_pk_fp8_f32 v2, v12, v13
	v_cvt_pk_fp8_f32 v6, v29, v30
	s_waitcnt lgkmcnt(0)
	v_sub_u32_e32 v3, v3, v5
	v_lshl_add_u32 v4, v4, 9, v3
	v_ashrrev_i32_e32 v5, 31, v4
	v_lshl_add_u64 v[4:5], v[4:5], 2, s[8:9]
	v_mov_b32_e32 v19, v211
	v_mov_b32_e32 v3, v147
	v_mov_b32_e32 v4, v147
	v_mov_b32_e32 v5, v147
	v_cvt_pk_fp8_f32 v3, v16, v17
	v_cvt_pk_fp8_f32 v4, v21, v22
	v_cvt_pk_fp8_f32 v5, v25, v26
	v_cvt_pk_fp8_f32 v7, v33, v34
	v_cvt_pk_fp8_f32 v8, v37, v38
	v_cvt_pk_fp8_f32 v9, v41, v42
	v_med3_f32 v14, v116, s45, v168
	v_med3_f32 v15, v117, s45, v168
	v_med3_f32 v18, v120, s45, v168
	v_med3_f32 v20, v121, s45, v168
	v_med3_f32 v23, v124, s45, v168
	v_med3_f32 v24, v125, s45, v168
	v_med3_f32 v27, v128, s45, v168
	v_med3_f32 v28, v129, s45, v168
	v_med3_f32 v31, v100, s45, v168
	v_med3_f32 v32, v101, s45, v168
	v_med3_f32 v35, v104, s45, v168
	v_med3_f32 v36, v105, s45, v168
	v_med3_f32 v39, v108, s45, v168
	v_med3_f32 v40, v109, s45, v168
	v_med3_f32 v43, v112, s45, v168
	v_med3_f32 v44, v113, s45, v168
	v_cvt_pk_fp8_f32 v2, v14, v15 op_sel:[0,0,1]
	v_cvt_pk_fp8_f32 v3, v18, v20 op_sel:[0,0,1]
	v_cvt_pk_fp8_f32 v4, v23, v24 op_sel:[0,0,1]
	v_cvt_pk_fp8_f32 v5, v27, v28 op_sel:[0,0,1]
	v_cvt_pk_fp8_f32 v6, v31, v32 op_sel:[0,0,1]
	v_cvt_pk_fp8_f32 v7, v35, v36 op_sel:[0,0,1]
	v_cvt_pk_fp8_f32 v8, v39, v40 op_sel:[0,0,1]
	v_cvt_pk_fp8_f32 v9, v43, v44 op_sel:[0,0,1]
	v_permlane32_swap_b32_e32 v2, v3
	v_permlane32_swap_b32_e32 v4, v5
	v_permlane32_swap_b32_e32 v6, v7
	v_permlane32_swap_b32_e32 v8, v9
	v_permlane32_swap_b32_e32 v2, v4
	v_permlane32_swap_b32_e32 v3, v5
	v_med3_f32 v53, v90, s45, v168
	v_permlane32_swap_b32_e32 v6, v8
	v_permlane32_swap_b32_e32 v7, v9
	v_med3_f32 v45, v82, s45, v168
	v_med3_f32 v46, v83, s45, v168
	v_mov_b32_e32 v10, v147
	v_med3_f32 v49, v86, s45, v168
	v_med3_f32 v50, v87, s45, v168
	v_mov_b32_e32 v11, v147
	v_cvt_pk_fp8_f32 v10, v45, v46
	v_cvt_pk_fp8_f32 v11, v49, v50
	v_med3_f32 v47, v84, s45, v168
	v_med3_f32 v48, v85, s45, v168
	v_med3_f32 v51, v88, s45, v168
	v_med3_f32 v52, v89, s45, v168
	v_cvt_pk_fp8_f32 v10, v47, v48 op_sel:[0,0,1]
	v_cvt_pk_fp8_f32 v11, v51, v52 op_sel:[0,0,1]
	s_waitcnt vmcnt(0)
	v_ashrrev_i32_e32 v12, 16, v19
	v_ashrrev_i32_e32 v13, 31, v12
	v_lshlrev_b32_e32 v14, 11, v19
	v_lshlrev_b64 v[12:13], 24, v[12:13]
	v_and_b32_e32 v146, 0x7fff800, v14
	v_lshl_add_u64 v[12:13], s[18:19], 0, v[12:13]
	v_lshl_add_u64 v[12:13], v[12:13], 0, v[146:147]
	v_lshl_add_u64 v[12:13], v[12:13], 0, s[30:31]
	v_lshl_add_u64 v[14:15], v[12:13], 0, v[150:151]
	global_store_dwordx4 v[14:15], v[2:5], off
	global_store_dwordx4 v[14:15], v[6:9], off offset:32
	v_mov_b32_e32 v12, v147
	v_med3_f32 v2, v91, s45, v168
	v_cvt_pk_fp8_f32 v12, v53, v2
	v_med3_f32 v2, v94, s45, v168
	v_med3_f32 v5, v95, s45, v168
	v_mov_b32_e32 v13, v147
	v_cvt_pk_fp8_f32 v13, v2, v5
	v_med3_f32 v3, v92, s45, v168
	v_med3_f32 v4, v93, s45, v168
	v_cvt_pk_fp8_f32 v12, v3, v4 op_sel:[0,0,1]
	v_med3_f32 v2, v96, s45, v168
	v_med3_f32 v3, v97, s45, v168
	v_cvt_pk_fp8_f32 v13, v2, v3 op_sel:[0,0,1]
	v_med3_f32 v3, v66, s45, v168
	v_med3_f32 v4, v67, s45, v168
	v_mov_b32_e32 v2, v147
	v_cvt_pk_fp8_f32 v2, v3, v4
	v_med3_f32 v4, v70, s45, v168
	v_med3_f32 v7, v71, s45, v168
	v_mov_b32_e32 v3, v147
	v_cvt_pk_fp8_f32 v3, v4, v7
	v_med3_f32 v5, v68, s45, v168
	v_med3_f32 v6, v69, s45, v168
	v_cvt_pk_fp8_f32 v2, v5, v6 op_sel:[0,0,1]
	v_med3_f32 v4, v72, s45, v168
	v_med3_f32 v5, v73, s45, v168
	v_cvt_pk_fp8_f32 v3, v4, v5 op_sel:[0,0,1]
	v_med3_f32 v5, v74, s45, v168
	v_med3_f32 v6, v75, s45, v168
	v_mov_b32_e32 v4, v147
	v_cvt_pk_fp8_f32 v4, v5, v6
	v_med3_f32 v6, v78, s45, v168
	v_med3_f32 v9, v79, s45, v168
	v_mov_b32_e32 v5, v147
	v_cvt_pk_fp8_f32 v5, v6, v9
	v_med3_f32 v7, v76, s45, v168
	v_med3_f32 v8, v77, s45, v168
	v_cvt_pk_fp8_f32 v4, v7, v8 op_sel:[0,0,1]
	v_med3_f32 v6, v80, s45, v168
	v_med3_f32 v7, v81, s45, v168
	v_cvt_pk_fp8_f32 v5, v6, v7 op_sel:[0,0,1]
	v_permlane32_swap_b32_e32 v10, v11
	v_permlane32_swap_b32_e32 v12, v13
	v_permlane32_swap_b32_e32 v2, v3
	v_permlane32_swap_b32_e32 v4, v5
	v_permlane32_swap_b32_e32 v10, v12
	v_permlane32_swap_b32_e32 v11, v13
	v_permlane32_swap_b32_e32 v2, v4
	v_permlane32_swap_b32_e32 v3, v5
	global_store_dwordx4 v[14:15], v[10:13], off offset:64
	global_store_dwordx4 v[14:15], v[2:5], off offset:96
	s_branch .LBB0_1082
